# plus: moe_combine row body issues all of a row's loads before the first use (counted vmcnt) instead of eight load-wait-store groups
# speedup vs baseline: 1.0079x; 1.0079x over previous
; template <int MODE>
; __device__ __forceinline__ void moe_combine(Frame& F, const float* gtf, int rank, int nrank, const LAS int* late) {
;     ...
;     for (int m = m0; m < m1; ++m) {
;         const int b = m >> 11, p1 = tk[TOK_POS + 2 * m], p2 = tk[TOK_POS + 2 * m + 1];
;         if (MODE != 0) { const bool is_late = (late[p1 >> 8] | late[p2 >> 8]) != 0; if ((MODE == 1) == is_late) continue; }
;         if (b != bcur) { bcur = b; const f32x4* gp0 = (const f32x4*)(gtf + (size_t)b * 12288) + F.lane;
; #pragma unroll
;             for (int j = 0; j < 8; ++j) gv[j] = gp0[64 * j]; }
;         const float w1 = __builtin_bit_cast(float, tk[TOK_W + 2 * m]), w2 = __builtin_bit_cast(float, tk[TOK_W + 2 * m + 1]);
;         const v2u* xr = (const v2u*)(xa + (size_t)m * DM) + F.lane;
;         const v2u* y1 = (const v2u*)(YS + (size_t)p1 * DM) + F.lane; const v2u* y2 = (const v2u*)(YS + (size_t)p2 * DM) + F.lane;
;         f32x4* op = (f32x4*)(F.out + (size_t)m * DM) + F.lane;
; #pragma unroll
;         for (int j = 0; j < 8; ++j) { const v2u xb = xr[64 * j]; const f32x4 g = gv[j]; const v2u a = y1[64 * j], c = y2[64 * j]; f32x4 x; x.x = bflo(xb.x); x.y = bfhi(xb.x); x.z = bflo(xb.y); x.w = bfhi(xb.y);
;             f32x4 y; y.x = w1 * bflo(a.x) + w2 * bflo(c.x); y.y = w1 * bfhi(a.x) + w2 * bfhi(c.x); y.z = w1 * bflo(a.y) + w2 * bflo(c.y); y.w = w1 * bfhi(a.y) + w2 * bfhi(c.y);
;             op[64 * j] = x + g * y; }
;     }
.LBB0_2114:
	v_ashrrev_i32_e32 v47, 31, v43
	v_mov_b32_e32 v46, v43
	v_ashrrev_i32_e32 v45, 31, v42
	v_mov_b32_e32 v44, v42
	v_lshlrev_b64 v[42:43], 12, v[46:47]
	v_lshlrev_b64 v[44:45], 12, v[44:45]
	v_lshl_add_u64 v[46:47], v[36:37], 0, v[42:43]
	v_lshl_add_u64 v[44:45], v[36:37], 0, v[44:45]
	global_load_dwordx2 v[52:53], v[38:39], off
	global_load_dwordx2 v[54:55], v[46:47], off
	global_load_dwordx2 v[56:57], v[44:45], off
	global_load_dwordx2 v[42:43], v49, s[14:15]
	global_load_dwordx2 v[68:69], v[38:39], off offset:512
	global_load_dwordx2 v[70:71], v[46:47], off offset:512
	global_load_dwordx2 v[72:73], v[44:45], off offset:512
	global_load_dwordx2 v[84:85], v[38:39], off offset:1024
	global_load_dwordx2 v[86:87], v[46:47], off offset:1024
	global_load_dwordx2 v[88:89], v[44:45], off offset:1024
	global_load_dwordx2 v[100:101], v[38:39], off offset:1536
	global_load_dwordx2 v[102:103], v[46:47], off offset:1536
	global_load_dwordx2 v[104:105], v[44:45], off offset:1536
	global_load_dwordx2 v[116:117], v[38:39], off offset:2048
	global_load_dwordx2 v[118:119], v[46:47], off offset:2048
	global_load_dwordx2 v[120:121], v[44:45], off offset:2048
	global_load_dwordx2 v[132:133], v[38:39], off offset:2560
	global_load_dwordx2 v[134:135], v[46:47], off offset:2560
	global_load_dwordx2 v[136:137], v[44:45], off offset:2560
	global_load_dwordx2 v[148:149], v[38:39], off offset:3072
	global_load_dwordx2 v[150:151], v[46:47], off offset:3072
	global_load_dwordx2 v[152:153], v[44:45], off offset:3072
	global_load_dwordx2 v[164:165], v[38:39], off offset:3584
	global_load_dwordx2 v[166:167], v[46:47], off offset:3584
	global_load_dwordx2 v[168:169], v[44:45], off offset:3584
	s_waitcnt vmcnt(23)
	v_lshlrev_b32_e32 v60, 16, v54
	s_waitcnt vmcnt(22)
	v_lshlrev_b32_e32 v62, 16, v56
	v_and_b32_e32 v63, 0xffff0000, v54
	v_lshlrev_b32_e32 v64, 16, v55
	v_lshlrev_b32_e32 v54, 16, v57
	v_and_b32_e32 v55, 0xffff0000, v55
	v_and_b32_e32 v61, 0xffff0000, v56
	v_and_b32_e32 v65, 0xffff0000, v57
	s_waitcnt vmcnt(21)
	v_pk_mul_f32 v[56:57], v[42:43], v[62:63]
	v_pk_mul_f32 v[54:55], v[42:43], v[54:55]
	v_lshlrev_b32_e32 v58, 16, v52
	v_and_b32_e32 v59, 0xffff0000, v52
	v_lshlrev_b32_e32 v52, 16, v53
	v_and_b32_e32 v53, 0xffff0000, v53
	v_pk_fma_f32 v[56:57], v[42:43], v[60:61], v[56:57] op_sel:[1,0,0] op_sel_hi:[0,1,1]
	v_pk_fma_f32 v[54:55], v[42:43], v[64:65], v[54:55] op_sel:[1,0,0] op_sel_hi:[0,1,1]
	v_pk_fma_f32 v[54:55], v[4:5], v[54:55], v[52:53]
	v_pk_fma_f32 v[52:53], v[2:3], v[56:57], v[58:59]
	global_store_dwordx4 v[40:41], v[52:55], off offset:-4096
	s_waitcnt vmcnt(21)
	v_lshlrev_b32_e32 v74, 16, v68
	s_waitcnt vmcnt(20)
	v_lshlrev_b32_e32 v76, 16, v70
	s_waitcnt vmcnt(19)
	v_lshlrev_b32_e32 v78, 16, v72
	v_and_b32_e32 v79, 0xffff0000, v70
	v_lshlrev_b32_e32 v80, 16, v71
	v_lshlrev_b32_e32 v70, 16, v73
	v_and_b32_e32 v71, 0xffff0000, v71
	v_and_b32_e32 v77, 0xffff0000, v72
	v_and_b32_e32 v81, 0xffff0000, v73
	v_pk_mul_f32 v[72:73], v[42:43], v[78:79]
	v_pk_mul_f32 v[70:71], v[42:43], v[70:71]
	v_and_b32_e32 v75, 0xffff0000, v68
	v_lshlrev_b32_e32 v68, 16, v69
	v_and_b32_e32 v69, 0xffff0000, v69
	v_pk_fma_f32 v[72:73], v[42:43], v[76:77], v[72:73] op_sel:[1,0,0] op_sel_hi:[0,1,1]
	v_pk_fma_f32 v[70:71], v[42:43], v[80:81], v[70:71] op_sel:[1,0,0] op_sel_hi:[0,1,1]
	v_pk_fma_f32 v[70:71], v[8:9], v[70:71], v[68:69]
	v_pk_fma_f32 v[68:69], v[6:7], v[72:73], v[74:75]
	global_store_dwordx4 v[40:41], v[68:71], off offset:-3072
	s_waitcnt vmcnt(19)
	v_lshlrev_b32_e32 v90, 16, v84
	s_waitcnt vmcnt(18)
	v_lshlrev_b32_e32 v92, 16, v86
	s_waitcnt vmcnt(17)
	v_lshlrev_b32_e32 v94, 16, v88
	v_and_b32_e32 v95, 0xffff0000, v86
	v_lshlrev_b32_e32 v96, 16, v87
	v_lshlrev_b32_e32 v86, 16, v89
	v_and_b32_e32 v87, 0xffff0000, v87
	v_and_b32_e32 v93, 0xffff0000, v88
	v_and_b32_e32 v97, 0xffff0000, v89
	v_pk_mul_f32 v[88:89], v[42:43], v[94:95]
	v_pk_mul_f32 v[86:87], v[42:43], v[86:87]
	v_and_b32_e32 v91, 0xffff0000, v84
	v_lshlrev_b32_e32 v84, 16, v85
	v_and_b32_e32 v85, 0xffff0000, v85
	v_pk_fma_f32 v[88:89], v[42:43], v[92:93], v[88:89] op_sel:[1,0,0] op_sel_hi:[0,1,1]
	v_pk_fma_f32 v[86:87], v[42:43], v[96:97], v[86:87] op_sel:[1,0,0] op_sel_hi:[0,1,1]
	v_pk_fma_f32 v[86:87], v[12:13], v[86:87], v[84:85]
	v_pk_fma_f32 v[84:85], v[10:11], v[88:89], v[90:91]
	global_store_dwordx4 v[40:41], v[84:87], off offset:-2048
	s_waitcnt vmcnt(17)
	v_lshlrev_b32_e32 v106, 16, v100
	s_waitcnt vmcnt(16)
	v_lshlrev_b32_e32 v108, 16, v102
	s_waitcnt vmcnt(15)
; template <int MODE>
; __device__ __forceinline__ void moe_combine(Frame& F, const float* gtf, int rank, int nrank, const LAS int* late) {
;     ...
;         for (int j = 0; j < 8; ++j) { const v2u xb = xr[64 * j]; const f32x4 g = gv[j]; const v2u a = y1[64 * j], c = y2[64 * j]; f32x4 x; x.x = bflo(xb.x); x.y = bfhi(xb.x); x.z = bflo(xb.y); x.w = bfhi(xb.y);
;             f32x4 y; y.x = w1 * bflo(a.x) + w2 * bflo(c.x); y.y = w1 * bfhi(a.x) + w2 * bfhi(c.x); y.z = w1 * bflo(a.y) + w2 * bflo(c.y); y.w = w1 * bfhi(a.y) + w2 * bfhi(c.y);
;             op[64 * j] = x + g * y; }
	v_lshlrev_b32_e32 v110, 16, v104
	v_and_b32_e32 v111, 0xffff0000, v102
	v_lshlrev_b32_e32 v112, 16, v103
	v_lshlrev_b32_e32 v102, 16, v105
	v_and_b32_e32 v103, 0xffff0000, v103
	v_and_b32_e32 v109, 0xffff0000, v104
	v_and_b32_e32 v113, 0xffff0000, v105
	v_pk_mul_f32 v[104:105], v[42:43], v[110:111]
	v_pk_mul_f32 v[102:103], v[42:43], v[102:103]
	v_and_b32_e32 v107, 0xffff0000, v100
	v_lshlrev_b32_e32 v100, 16, v101
	v_and_b32_e32 v101, 0xffff0000, v101
	v_pk_fma_f32 v[104:105], v[42:43], v[108:109], v[104:105] op_sel:[1,0,0] op_sel_hi:[0,1,1]
	v_pk_fma_f32 v[102:103], v[42:43], v[112:113], v[102:103] op_sel:[1,0,0] op_sel_hi:[0,1,1]
	v_pk_fma_f32 v[102:103], v[16:17], v[102:103], v[100:101]
	v_pk_fma_f32 v[100:101], v[14:15], v[104:105], v[106:107]
	global_store_dwordx4 v[40:41], v[100:103], off offset:-1024
	s_waitcnt vmcnt(15)
	v_lshlrev_b32_e32 v122, 16, v116
	s_waitcnt vmcnt(14)
	v_lshlrev_b32_e32 v124, 16, v118
	s_waitcnt vmcnt(13)
	v_lshlrev_b32_e32 v126, 16, v120
	v_and_b32_e32 v127, 0xffff0000, v118
	v_lshlrev_b32_e32 v128, 16, v119
	v_lshlrev_b32_e32 v118, 16, v121
	v_and_b32_e32 v119, 0xffff0000, v119
	v_and_b32_e32 v125, 0xffff0000, v120
	v_and_b32_e32 v129, 0xffff0000, v121
	v_pk_mul_f32 v[120:121], v[42:43], v[126:127]
	v_pk_mul_f32 v[118:119], v[42:43], v[118:119]
	v_and_b32_e32 v123, 0xffff0000, v116
	v_lshlrev_b32_e32 v116, 16, v117
	v_and_b32_e32 v117, 0xffff0000, v117
	v_pk_fma_f32 v[120:121], v[42:43], v[124:125], v[120:121] op_sel:[1,0,0] op_sel_hi:[0,1,1]
	v_pk_fma_f32 v[118:119], v[42:43], v[128:129], v[118:119] op_sel:[1,0,0] op_sel_hi:[0,1,1]
	v_pk_fma_f32 v[118:119], v[20:21], v[118:119], v[116:117]
	v_pk_fma_f32 v[116:117], v[18:19], v[120:121], v[122:123]
	global_store_dwordx4 v[40:41], v[116:119], off
	s_waitcnt vmcnt(13)
	v_lshlrev_b32_e32 v138, 16, v132
	s_waitcnt vmcnt(12)
	v_lshlrev_b32_e32 v140, 16, v134
	s_waitcnt vmcnt(11)
	v_lshlrev_b32_e32 v142, 16, v136
	v_and_b32_e32 v143, 0xffff0000, v134
	v_lshlrev_b32_e32 v144, 16, v135
	v_lshlrev_b32_e32 v134, 16, v137
	v_and_b32_e32 v135, 0xffff0000, v135
	v_and_b32_e32 v141, 0xffff0000, v136
	v_and_b32_e32 v145, 0xffff0000, v137
	v_pk_mul_f32 v[136:137], v[42:43], v[142:143]
	v_pk_mul_f32 v[134:135], v[42:43], v[134:135]
	v_and_b32_e32 v139, 0xffff0000, v132
	v_lshlrev_b32_e32 v132, 16, v133
	v_and_b32_e32 v133, 0xffff0000, v133
	v_pk_fma_f32 v[136:137], v[42:43], v[140:141], v[136:137] op_sel:[1,0,0] op_sel_hi:[0,1,1]
	v_pk_fma_f32 v[134:135], v[42:43], v[144:145], v[134:135] op_sel:[1,0,0] op_sel_hi:[0,1,1]
	v_pk_fma_f32 v[134:135], v[24:25], v[134:135], v[132:133]
	v_pk_fma_f32 v[132:133], v[22:23], v[136:137], v[138:139]
	global_store_dwordx4 v[40:41], v[132:135], off offset:1024
	s_waitcnt vmcnt(11)
	v_lshlrev_b32_e32 v154, 16, v148
	s_waitcnt vmcnt(10)
	v_lshlrev_b32_e32 v156, 16, v150
	s_waitcnt vmcnt(9)
	v_lshlrev_b32_e32 v158, 16, v152
	v_and_b32_e32 v159, 0xffff0000, v150
	v_lshlrev_b32_e32 v160, 16, v151
	v_lshlrev_b32_e32 v150, 16, v153
	v_and_b32_e32 v151, 0xffff0000, v151
	v_and_b32_e32 v157, 0xffff0000, v152
	v_and_b32_e32 v161, 0xffff0000, v153
	v_pk_mul_f32 v[152:153], v[42:43], v[158:159]
	v_pk_mul_f32 v[150:151], v[42:43], v[150:151]
	v_and_b32_e32 v155, 0xffff0000, v148
	v_lshlrev_b32_e32 v148, 16, v149
	v_and_b32_e32 v149, 0xffff0000, v149
	v_pk_fma_f32 v[152:153], v[42:43], v[156:157], v[152:153] op_sel:[1,0,0] op_sel_hi:[0,1,1]
	v_pk_fma_f32 v[150:151], v[42:43], v[160:161], v[150:151] op_sel:[1,0,0] op_sel_hi:[0,1,1]
	v_pk_fma_f32 v[150:151], v[28:29], v[150:151], v[148:149]
	v_pk_fma_f32 v[148:149], v[26:27], v[152:153], v[154:155]
	global_store_dwordx4 v[40:41], v[148:151], off offset:2048
	s_waitcnt vmcnt(9)
	v_lshlrev_b32_e32 v46, 16, v164
	v_and_b32_e32 v47, 0xffff0000, v164
	s_waitcnt vmcnt(8)
	v_lshlrev_b32_e32 v164, 16, v166
	s_waitcnt vmcnt(7)
	v_lshlrev_b32_e32 v170, 16, v168
	v_and_b32_e32 v171, 0xffff0000, v166
	v_lshlrev_b32_e32 v172, 16, v167
	v_lshlrev_b32_e32 v166, 16, v169
	v_and_b32_e32 v167, 0xffff0000, v167
	v_lshlrev_b32_e32 v44, 16, v165
	v_and_b32_e32 v45, 0xffff0000, v165
	v_and_b32_e32 v165, 0xffff0000, v168
	v_and_b32_e32 v173, 0xffff0000, v169
	v_pk_mul_f32 v[168:169], v[42:43], v[170:171]
	v_pk_mul_f32 v[166:167], v[42:43], v[166:167]
	v_pk_fma_f32 v[164:165], v[42:43], v[164:165], v[168:169] op_sel:[1,0,0] op_sel_hi:[0,1,1]
	v_pk_fma_f32 v[42:43], v[42:43], v[172:173], v[166:167] op_sel:[1,0,0] op_sel_hi:[0,1,1]
	v_pk_fma_f32 v[44:45], v[32:33], v[42:43], v[44:45]
	v_pk_fma_f32 v[42:43], v[30:31], v[164:165], v[46:47]
	global_store_dwordx4 v[40:41], v[42:45], off offset:3072

; template <int MODE>
; __device__ __forceinline__ void moe_combine(Frame& F, const float* gtf, int rank, int nrank, const LAS int* late) {
;     ...
;     for (int m = m0; m < m1; ++m) {
;         const int b = m >> 11, p1 = tk[TOK_POS + 2 * m], p2 = tk[TOK_POS + 2 * m + 1];
;         if (MODE != 0) { const bool is_late = (late[p1 >> 8] | late[p2 >> 8]) != 0; if ((MODE == 1) == is_late) continue; }
;         if (b != bcur) { bcur = b; const f32x4* gp0 = (const f32x4*)(gtf + (size_t)b * 12288) + F.lane;
; #pragma unroll
;             for (int j = 0; j < 8; ++j) gv[j] = gp0[64 * j]; }
;         const float w1 = __builtin_bit_cast(float, tk[TOK_W + 2 * m]), w2 = __builtin_bit_cast(float, tk[TOK_W + 2 * m + 1]);
;         const v2u* xr = (const v2u*)(xa + (size_t)m * DM) + F.lane;
;         const v2u* y1 = (const v2u*)(YS + (size_t)p1 * DM) + F.lane; const v2u* y2 = (const v2u*)(YS + (size_t)p2 * DM) + F.lane;
;         f32x4* op = (f32x4*)(F.out + (size_t)m * DM) + F.lane;
; #pragma unroll
;         for (int j = 0; j < 8; ++j) { const v2u xb = xr[64 * j]; const f32x4 g = gv[j]; const v2u a = y1[64 * j], c = y2[64 * j]; f32x4 x; x.x = bflo(xb.x); x.y = bfhi(xb.x); x.z = bflo(xb.y); x.w = bfhi(xb.y);
;             f32x4 y; y.x = w1 * bflo(a.x) + w2 * bflo(c.x); y.y = w1 * bfhi(a.x) + w2 * bfhi(c.x); y.z = w1 * bflo(a.y) + w2 * bflo(c.y); y.w = w1 * bfhi(a.y) + w2 * bfhi(c.y);
;             op[64 * j] = x + g * y; }
;     }
.LBB0_2193:
	v_ashrrev_i32_e32 v45, 31, v41
	v_mov_b32_e32 v44, v41
	v_ashrrev_i32_e32 v43, 31, v40
	v_mov_b32_e32 v42, v40
	v_lshlrev_b64 v[40:41], 12, v[44:45]
	v_lshlrev_b64 v[42:43], 12, v[42:43]
	v_lshl_add_u64 v[44:45], v[34:35], 0, v[40:41]
	v_lshl_add_u64 v[42:43], v[34:35], 0, v[42:43]
	global_load_dwordx2 v[50:51], v[36:37], off
	global_load_dwordx2 v[52:53], v[44:45], off
	global_load_dwordx2 v[54:55], v[42:43], off
	global_load_dwordx2 v[40:41], v47, s[8:9]
	global_load_dwordx2 v[66:67], v[36:37], off offset:512
	global_load_dwordx2 v[68:69], v[44:45], off offset:512
	global_load_dwordx2 v[70:71], v[42:43], off offset:512
	global_load_dwordx2 v[82:83], v[36:37], off offset:1024
	global_load_dwordx2 v[84:85], v[44:45], off offset:1024
	global_load_dwordx2 v[86:87], v[42:43], off offset:1024
	global_load_dwordx2 v[98:99], v[36:37], off offset:1536
	global_load_dwordx2 v[100:101], v[44:45], off offset:1536
	global_load_dwordx2 v[102:103], v[42:43], off offset:1536
	global_load_dwordx2 v[114:115], v[36:37], off offset:2048
	global_load_dwordx2 v[116:117], v[44:45], off offset:2048
	global_load_dwordx2 v[118:119], v[42:43], off offset:2048
	global_load_dwordx2 v[130:131], v[36:37], off offset:2560
	global_load_dwordx2 v[132:133], v[44:45], off offset:2560
	global_load_dwordx2 v[134:135], v[42:43], off offset:2560
	global_load_dwordx2 v[146:147], v[36:37], off offset:3072
	global_load_dwordx2 v[148:149], v[44:45], off offset:3072
	global_load_dwordx2 v[150:151], v[42:43], off offset:3072
	global_load_dwordx2 v[162:163], v[36:37], off offset:3584
	global_load_dwordx2 v[164:165], v[44:45], off offset:3584
	global_load_dwordx2 v[166:167], v[42:43], off offset:3584
	s_waitcnt vmcnt(23)
	v_lshlrev_b32_e32 v58, 16, v52
	s_waitcnt vmcnt(22)
	v_lshlrev_b32_e32 v60, 16, v54
	v_and_b32_e32 v61, 0xffff0000, v52
	v_lshlrev_b32_e32 v62, 16, v53
	v_lshlrev_b32_e32 v52, 16, v55
	v_and_b32_e32 v53, 0xffff0000, v53
	v_and_b32_e32 v59, 0xffff0000, v54
	v_and_b32_e32 v63, 0xffff0000, v55
	s_waitcnt vmcnt(21)
	v_pk_mul_f32 v[54:55], v[40:41], v[60:61]
	v_pk_mul_f32 v[52:53], v[40:41], v[52:53]
	v_lshlrev_b32_e32 v56, 16, v50
	v_and_b32_e32 v57, 0xffff0000, v50
	v_lshlrev_b32_e32 v50, 16, v51
	v_and_b32_e32 v51, 0xffff0000, v51
	v_pk_fma_f32 v[54:55], v[40:41], v[58:59], v[54:55] op_sel:[1,0,0] op_sel_hi:[0,1,1]
	v_pk_fma_f32 v[52:53], v[40:41], v[62:63], v[52:53] op_sel:[1,0,0] op_sel_hi:[0,1,1]
	v_pk_fma_f32 v[52:53], v[2:3], v[52:53], v[50:51]
	v_pk_fma_f32 v[50:51], v[0:1], v[54:55], v[56:57]
	global_store_dwordx4 v[38:39], v[50:53], off offset:-4096
	s_waitcnt vmcnt(21)
	v_lshlrev_b32_e32 v72, 16, v66
	s_waitcnt vmcnt(20)
	v_lshlrev_b32_e32 v74, 16, v68
	s_waitcnt vmcnt(19)
	v_lshlrev_b32_e32 v76, 16, v70
	v_and_b32_e32 v77, 0xffff0000, v68
	v_lshlrev_b32_e32 v78, 16, v69
	v_lshlrev_b32_e32 v68, 16, v71
	v_and_b32_e32 v69, 0xffff0000, v69
	v_and_b32_e32 v75, 0xffff0000, v70
	v_and_b32_e32 v79, 0xffff0000, v71
	v_pk_mul_f32 v[70:71], v[40:41], v[76:77]
	v_pk_mul_f32 v[68:69], v[40:41], v[68:69]
	v_and_b32_e32 v73, 0xffff0000, v66
	v_lshlrev_b32_e32 v66, 16, v67
	v_and_b32_e32 v67, 0xffff0000, v67
	v_pk_fma_f32 v[70:71], v[40:41], v[74:75], v[70:71] op_sel:[1,0,0] op_sel_hi:[0,1,1]
	v_pk_fma_f32 v[68:69], v[40:41], v[78:79], v[68:69] op_sel:[1,0,0] op_sel_hi:[0,1,1]
	v_pk_fma_f32 v[68:69], v[6:7], v[68:69], v[66:67]
	v_pk_fma_f32 v[66:67], v[4:5], v[70:71], v[72:73]
	global_store_dwordx4 v[38:39], v[66:69], off offset:-3072
	s_waitcnt vmcnt(19)
	v_lshlrev_b32_e32 v88, 16, v82
	s_waitcnt vmcnt(18)
	v_lshlrev_b32_e32 v90, 16, v84
	s_waitcnt vmcnt(17)
	v_lshlrev_b32_e32 v92, 16, v86
	v_and_b32_e32 v93, 0xffff0000, v84
	v_lshlrev_b32_e32 v94, 16, v85
	v_lshlrev_b32_e32 v84, 16, v87
	v_and_b32_e32 v85, 0xffff0000, v85
	v_and_b32_e32 v91, 0xffff0000, v86
	v_and_b32_e32 v95, 0xffff0000, v87
	v_pk_mul_f32 v[86:87], v[40:41], v[92:93]
	v_pk_mul_f32 v[84:85], v[40:41], v[84:85]
	v_and_b32_e32 v89, 0xffff0000, v82
	v_lshlrev_b32_e32 v82, 16, v83
	v_and_b32_e32 v83, 0xffff0000, v83
	v_pk_fma_f32 v[86:87], v[40:41], v[90:91], v[86:87] op_sel:[1,0,0] op_sel_hi:[0,1,1]
	v_pk_fma_f32 v[84:85], v[40:41], v[94:95], v[84:85] op_sel:[1,0,0] op_sel_hi:[0,1,1]
	v_pk_fma_f32 v[84:85], v[10:11], v[84:85], v[82:83]
	v_pk_fma_f32 v[82:83], v[8:9], v[86:87], v[88:89]
	global_store_dwordx4 v[38:39], v[82:85], off offset:-2048
	s_waitcnt vmcnt(17)
	v_lshlrev_b32_e32 v104, 16, v98
	s_waitcnt vmcnt(16)
	v_lshlrev_b32_e32 v106, 16, v100
	s_waitcnt vmcnt(15)
; template <int MODE>
; __device__ __forceinline__ void moe_combine(Frame& F, const float* gtf, int rank, int nrank, const LAS int* late) {
;     ...
;         for (int j = 0; j < 8; ++j) { const v2u xb = xr[64 * j]; const f32x4 g = gv[j]; const v2u a = y1[64 * j], c = y2[64 * j]; f32x4 x; x.x = bflo(xb.x); x.y = bfhi(xb.x); x.z = bflo(xb.y); x.w = bfhi(xb.y);
;             f32x4 y; y.x = w1 * bflo(a.x) + w2 * bflo(c.x); y.y = w1 * bfhi(a.x) + w2 * bfhi(c.x); y.z = w1 * bflo(a.y) + w2 * bflo(c.y); y.w = w1 * bfhi(a.y) + w2 * bfhi(c.y);
;             op[64 * j] = x + g * y; }
	v_lshlrev_b32_e32 v108, 16, v102
	v_and_b32_e32 v109, 0xffff0000, v100
	v_lshlrev_b32_e32 v110, 16, v101
	v_lshlrev_b32_e32 v100, 16, v103
	v_and_b32_e32 v101, 0xffff0000, v101
	v_and_b32_e32 v107, 0xffff0000, v102
	v_and_b32_e32 v111, 0xffff0000, v103
	v_pk_mul_f32 v[102:103], v[40:41], v[108:109]
	v_pk_mul_f32 v[100:101], v[40:41], v[100:101]
	v_and_b32_e32 v105, 0xffff0000, v98
	v_lshlrev_b32_e32 v98, 16, v99
	v_and_b32_e32 v99, 0xffff0000, v99
	v_pk_fma_f32 v[102:103], v[40:41], v[106:107], v[102:103] op_sel:[1,0,0] op_sel_hi:[0,1,1]
	v_pk_fma_f32 v[100:101], v[40:41], v[110:111], v[100:101] op_sel:[1,0,0] op_sel_hi:[0,1,1]
	v_pk_fma_f32 v[100:101], v[14:15], v[100:101], v[98:99]
	v_pk_fma_f32 v[98:99], v[12:13], v[102:103], v[104:105]
	global_store_dwordx4 v[38:39], v[98:101], off offset:-1024
	s_waitcnt vmcnt(15)
	v_lshlrev_b32_e32 v120, 16, v114
	s_waitcnt vmcnt(14)
	v_lshlrev_b32_e32 v122, 16, v116
	s_waitcnt vmcnt(13)
	v_lshlrev_b32_e32 v124, 16, v118
	v_and_b32_e32 v125, 0xffff0000, v116
	v_lshlrev_b32_e32 v126, 16, v117
	v_lshlrev_b32_e32 v116, 16, v119
	v_and_b32_e32 v117, 0xffff0000, v117
	v_and_b32_e32 v123, 0xffff0000, v118
	v_and_b32_e32 v127, 0xffff0000, v119
	v_pk_mul_f32 v[118:119], v[40:41], v[124:125]
	v_pk_mul_f32 v[116:117], v[40:41], v[116:117]
	v_and_b32_e32 v121, 0xffff0000, v114
	v_lshlrev_b32_e32 v114, 16, v115
	v_and_b32_e32 v115, 0xffff0000, v115
	v_pk_fma_f32 v[118:119], v[40:41], v[122:123], v[118:119] op_sel:[1,0,0] op_sel_hi:[0,1,1]
	v_pk_fma_f32 v[116:117], v[40:41], v[126:127], v[116:117] op_sel:[1,0,0] op_sel_hi:[0,1,1]
	v_pk_fma_f32 v[116:117], v[18:19], v[116:117], v[114:115]
	v_pk_fma_f32 v[114:115], v[16:17], v[118:119], v[120:121]
	global_store_dwordx4 v[38:39], v[114:117], off
	s_waitcnt vmcnt(13)
	v_lshlrev_b32_e32 v136, 16, v130
	s_waitcnt vmcnt(12)
	v_lshlrev_b32_e32 v138, 16, v132
	s_waitcnt vmcnt(11)
	v_lshlrev_b32_e32 v140, 16, v134
	v_and_b32_e32 v141, 0xffff0000, v132
	v_lshlrev_b32_e32 v142, 16, v133
	v_lshlrev_b32_e32 v132, 16, v135
	v_and_b32_e32 v133, 0xffff0000, v133
	v_and_b32_e32 v139, 0xffff0000, v134
	v_and_b32_e32 v143, 0xffff0000, v135
	v_pk_mul_f32 v[134:135], v[40:41], v[140:141]
	v_pk_mul_f32 v[132:133], v[40:41], v[132:133]
	v_and_b32_e32 v137, 0xffff0000, v130
	v_lshlrev_b32_e32 v130, 16, v131
	v_and_b32_e32 v131, 0xffff0000, v131
	v_pk_fma_f32 v[134:135], v[40:41], v[138:139], v[134:135] op_sel:[1,0,0] op_sel_hi:[0,1,1]
	v_pk_fma_f32 v[132:133], v[40:41], v[142:143], v[132:133] op_sel:[1,0,0] op_sel_hi:[0,1,1]
	v_pk_fma_f32 v[132:133], v[22:23], v[132:133], v[130:131]
	v_pk_fma_f32 v[130:131], v[20:21], v[134:135], v[136:137]
	global_store_dwordx4 v[38:39], v[130:133], off offset:1024
	s_waitcnt vmcnt(11)
	v_lshlrev_b32_e32 v152, 16, v146
	s_waitcnt vmcnt(10)
	v_lshlrev_b32_e32 v154, 16, v148
	s_waitcnt vmcnt(9)
	v_lshlrev_b32_e32 v156, 16, v150
	v_and_b32_e32 v157, 0xffff0000, v148
	v_lshlrev_b32_e32 v158, 16, v149
	v_lshlrev_b32_e32 v148, 16, v151
	v_and_b32_e32 v149, 0xffff0000, v149
	v_and_b32_e32 v155, 0xffff0000, v150
	v_and_b32_e32 v159, 0xffff0000, v151
	v_pk_mul_f32 v[150:151], v[40:41], v[156:157]
	v_pk_mul_f32 v[148:149], v[40:41], v[148:149]
	v_and_b32_e32 v153, 0xffff0000, v146
	v_lshlrev_b32_e32 v146, 16, v147
	v_and_b32_e32 v147, 0xffff0000, v147
	v_pk_fma_f32 v[150:151], v[40:41], v[154:155], v[150:151] op_sel:[1,0,0] op_sel_hi:[0,1,1]
	v_pk_fma_f32 v[148:149], v[40:41], v[158:159], v[148:149] op_sel:[1,0,0] op_sel_hi:[0,1,1]
	v_pk_fma_f32 v[148:149], v[26:27], v[148:149], v[146:147]
	v_pk_fma_f32 v[146:147], v[24:25], v[150:151], v[152:153]
	global_store_dwordx4 v[38:39], v[146:149], off offset:2048
	s_waitcnt vmcnt(9)
	v_lshlrev_b32_e32 v44, 16, v162
	v_and_b32_e32 v45, 0xffff0000, v162
	s_waitcnt vmcnt(8)
	v_lshlrev_b32_e32 v162, 16, v164
	s_waitcnt vmcnt(7)
	v_lshlrev_b32_e32 v168, 16, v166
	v_and_b32_e32 v169, 0xffff0000, v164
	v_lshlrev_b32_e32 v170, 16, v165
	v_lshlrev_b32_e32 v164, 16, v167
	v_and_b32_e32 v165, 0xffff0000, v165
	v_lshlrev_b32_e32 v42, 16, v163
	v_and_b32_e32 v43, 0xffff0000, v163
	v_and_b32_e32 v163, 0xffff0000, v166
	v_and_b32_e32 v171, 0xffff0000, v167
	v_pk_mul_f32 v[166:167], v[40:41], v[168:169]
	v_pk_mul_f32 v[164:165], v[40:41], v[164:165]
	v_pk_fma_f32 v[162:163], v[40:41], v[162:163], v[166:167] op_sel:[1,0,0] op_sel_hi:[0,1,1]
	v_pk_fma_f32 v[40:41], v[40:41], v[170:171], v[164:165] op_sel:[1,0,0] op_sel_hi:[0,1,1]
	v_pk_fma_f32 v[42:43], v[30:31], v[40:41], v[42:43]
	v_pk_fma_f32 v[40:41], v[28:29], v[162:163], v[44:45]
	global_store_dwordx4 v[38:39], v[40:43], off offset:3072
